# v88 variant: partner class = vcu^0x81 (uniform 23 items per convert-first wave)
# baseline (speedup 1.0000x reference)
; #define CV_LOAD(c) do { _Pragma("unroll") for (int nh = 0; nh < 2; ++nh) _Pragma("unroll") for (int q = 0; q < 4; ++q) { const float* p_ = (c).src + (size_t)(krow + 4 * q) * (c).N + 32 * nh + 8 * lg; \
;         v[(nh * 4 + q) * 2] = *(const f32x4*)p_; v[(nh * 4 + q) * 2 + 1] = *(const f32x4*)(p_ + 4); } } while (0)
; __device__ __forceinline__ void p2_convert_experts(Ctx& F) {
;     const int gw = F.vcu * NWAVES + F.wave, NGW = F.G * NWAVES, lane = F.lane, li = lane & 15, lg = lane >> 4;
;     constexpr int NCV = 65 * (32 * 16 + 8 * 32);
;     int it = gw; CvItem cur; f32x4 v[16];
;     const int krow = 16 * (li >> 2) + (li & 3);
;     ...
;     if (it < NCV) { cur = cv_decode(F.in, F.ws, it); CV_LOAD(cur); }
;     while (it < NCV) {
.LBB0_191:
	s_cmp_lg_u32 s101, 0
	s_cbranch_scc1 .Lcv1_done
	s_mov_b32 s101, 1
	s_xor_b32 s3, s85, 0x81
	s_lshl_b32 s3, s3, 3
	s_add_i32 s3, s3, s67
	s_add_i32 s3, s3, 0x8000
	s_branch .Lcv1_reenter
